# mixer HGRN2 stages 1 and 2 re-emitted with packed f32 arithmetic on position pairs (same operations and order per element), on top of the early done signal
# speedup vs baseline: 1.0277x; 1.0017x over previous
.LBB0_466:
	v_cndmask_b32_e64 v2, 0, 1, s[38:39]
	v_cmp_ne_u32_e64 s[78:79], 1, v2
	s_andn2_b64 vcc, exec, s[38:39]
	s_mov_b64 s[8:9], -1
	s_cbranch_vccnz .LBB0_468
	v_add_u32_e32 v8, s94, v106
	v_add_u32_e32 v16, s94, v105
	ds_read2st64_b32 v[2:3], v8 offset1:1
	ds_read2st64_b32 v[4:5], v8 offset0:2 offset1:3
	ds_read2st64_b32 v[6:7], v8 offset0:4 offset1:5
	ds_read2st64_b32 v[8:9], v8 offset0:6 offset1:7
	ds_read2st64_b32 v[10:11], v16 offset1:1
	ds_read2st64_b32 v[12:13], v16 offset0:2 offset1:3
	ds_read2st64_b32 v[14:15], v16 offset0:4 offset1:5
	ds_read2st64_b32 v[16:17], v16 offset0:6 offset1:7
	s_mov_b64 s[8:9], 0
	s_mov_b32 s98, 0xbfb8aa3b
	s_waitcnt lgkmcnt(4)
	v_lshlrev_b32_e32 v56, 16, v2
	v_and_b32_e32 v64, 0xffff0000, v2
	v_lshlrev_b32_e32 v57, 16, v3
	v_and_b32_e32 v65, 0xffff0000, v3
	v_lshlrev_b32_e32 v58, 16, v4
	v_and_b32_e32 v66, 0xffff0000, v4
	v_lshlrev_b32_e32 v59, 16, v5
	v_and_b32_e32 v67, 0xffff0000, v5
	v_lshlrev_b32_e32 v60, 16, v6
	v_and_b32_e32 v68, 0xffff0000, v6
	v_lshlrev_b32_e32 v61, 16, v7
	v_and_b32_e32 v69, 0xffff0000, v7
	v_lshlrev_b32_e32 v62, 16, v8
	v_and_b32_e32 v70, 0xffff0000, v8
	v_lshlrev_b32_e32 v63, 16, v9
	v_and_b32_e32 v71, 0xffff0000, v9
	v_pk_mul_f32 v[56:57], v[56:57], s[98:99] op_sel_hi:[1,0]
	v_pk_mul_f32 v[64:65], v[64:65], s[98:99] op_sel_hi:[1,0]
	v_pk_mul_f32 v[58:59], v[58:59], s[98:99] op_sel_hi:[1,0]
	v_pk_mul_f32 v[66:67], v[66:67], s[98:99] op_sel_hi:[1,0]
	v_pk_mul_f32 v[60:61], v[60:61], s[98:99] op_sel_hi:[1,0]
	v_pk_mul_f32 v[68:69], v[68:69], s[98:99] op_sel_hi:[1,0]
	v_pk_mul_f32 v[62:63], v[62:63], s[98:99] op_sel_hi:[1,0]
	v_pk_mul_f32 v[70:71], v[70:71], s[98:99] op_sel_hi:[1,0]
	v_exp_f32_e32 v56, v56
	v_exp_f32_e32 v64, v64
	v_exp_f32_e32 v57, v57
	v_exp_f32_e32 v65, v65
	v_exp_f32_e32 v58, v58
	v_exp_f32_e32 v66, v66
	v_exp_f32_e32 v59, v59
	v_exp_f32_e32 v67, v67
	v_exp_f32_e32 v60, v60
	v_exp_f32_e32 v68, v68
	v_exp_f32_e32 v61, v61
	v_exp_f32_e32 v69, v69
	v_exp_f32_e32 v62, v62
	v_exp_f32_e32 v70, v70
	v_exp_f32_e32 v63, v63
	v_exp_f32_e32 v71, v71
	s_waitcnt lgkmcnt(0)
	s_cmpk_eq_i32 s4, 0x7c0
	s_cbranch_scc1 .Lmx_qk_skip_h
	v_add_u32_e32 v176, s4, v110
	v_add_u32_e32 v177, s24, v121
	v_add_u32_e32 v178, 64, v176
	v_add_u32_e32 v179, 0x7bf, v177
	v_cndmask_b32_e64 v178, v179, v178, s[76:77]
	v_add_u32_e32 v178, s84, v178
	v_mad_i64_i32 v[178:179], s[100:101], v178, s20, v[38:39]
	s_mov_b32 m0, s19
	v_lshl_add_u64 v[180:181], v[178:179], 0, s[80:81]
	global_load_lds_dwordx4 v[180:181], off
	v_lshl_add_u64 v[178:179], v[178:179], 0, s[6:7]
	s_mov_b32 m0, s82
	v_add_u32_e32 v176, 0x44, v176
	global_load_lds_dwordx4 v[178:179], off
	v_add_u32_e32 v178, 0x7bb, v177
	v_cndmask_b32_e64 v176, v178, v176, s[76:77]
	v_add_u32_e32 v176, s84, v176
	v_mad_i64_i32 v[178:179], s[100:101], v176, s20, v[38:39]
	v_lshl_add_u64 v[180:181], v[178:179], 0, s[80:81]
	s_mov_b32 m0, s85
	v_lshl_add_u64 v[178:179], v[178:179], 0, s[6:7]
	global_load_lds_dwordx4 v[180:181], off
	s_mov_b32 m0, s86
	s_nop 0
	global_load_lds_dwordx4 v[178:179], off
.Lmx_qk_skip_h:
	v_lshlrev_b32_e32 v200, 16, v10
	v_and_b32_e32 v208, 0xffff0000, v10
	v_lshlrev_b32_e32 v201, 16, v11
	v_and_b32_e32 v209, 0xffff0000, v11
	v_lshlrev_b32_e32 v202, 16, v12
	v_and_b32_e32 v210, 0xffff0000, v12
	v_lshlrev_b32_e32 v203, 16, v13
	v_and_b32_e32 v211, 0xffff0000, v13
	v_lshlrev_b32_e32 v204, 16, v14
	v_and_b32_e32 v212, 0xffff0000, v14
	v_lshlrev_b32_e32 v205, 16, v15
	v_and_b32_e32 v213, 0xffff0000, v15
	v_lshlrev_b32_e32 v206, 16, v16
	v_and_b32_e32 v214, 0xffff0000, v16
	v_lshlrev_b32_e32 v207, 16, v17
	v_and_b32_e32 v215, 0xffff0000, v17
	v_pk_add_f32 v[56:57], v[56:57], 1.0 op_sel_hi:[1,0]
	v_pk_add_f32 v[64:65], v[64:65], 1.0 op_sel_hi:[1,0]
	v_pk_add_f32 v[58:59], v[58:59], 1.0 op_sel_hi:[1,0]
	v_pk_add_f32 v[66:67], v[66:67], 1.0 op_sel_hi:[1,0]
	v_pk_add_f32 v[60:61], v[60:61], 1.0 op_sel_hi:[1,0]
	v_pk_add_f32 v[68:69], v[68:69], 1.0 op_sel_hi:[1,0]
	v_pk_add_f32 v[62:63], v[62:63], 1.0 op_sel_hi:[1,0]
	v_pk_add_f32 v[70:71], v[70:71], 1.0 op_sel_hi:[1,0]
	v_rcp_f32_e32 v56, v56
	v_rcp_f32_e32 v64, v64
	v_rcp_f32_e32 v57, v57
	v_rcp_f32_e32 v65, v65
	v_rcp_f32_e32 v58, v58
	v_rcp_f32_e32 v66, v66
	v_rcp_f32_e32 v59, v59
	v_rcp_f32_e32 v67, v67
	v_rcp_f32_e32 v60, v60
	v_rcp_f32_e32 v68, v68
	v_rcp_f32_e32 v61, v61
	v_rcp_f32_e32 v69, v69
	v_rcp_f32_e32 v62, v62
	v_rcp_f32_e32 v70, v70
	v_rcp_f32_e32 v63, v63
	v_rcp_f32_e32 v71, v71
	v_pk_fma_f32 v[56:57], v[56:57], v[44:45], v[140:141] op_sel:[0,1,0] op_sel_hi:[1,1,0]
	v_pk_fma_f32 v[64:65], v[64:65], v[142:143], v[138:139] op_sel:[0,1,1] op_sel_hi:[1,1,1]
	v_pk_fma_f32 v[58:59], v[58:59], v[44:45], v[140:141] op_sel:[0,1,0] op_sel_hi:[1,1,0]
	v_pk_fma_f32 v[66:67], v[66:67], v[142:143], v[138:139] op_sel:[0,1,1] op_sel_hi:[1,1,1]
	v_pk_fma_f32 v[60:61], v[60:61], v[44:45], v[140:141] op_sel:[0,1,0] op_sel_hi:[1,1,0]
	v_pk_fma_f32 v[68:69], v[68:69], v[142:143], v[138:139] op_sel:[0,1,1] op_sel_hi:[1,1,1]
	v_pk_fma_f32 v[62:63], v[62:63], v[44:45], v[140:141] op_sel:[0,1,0] op_sel_hi:[1,1,0]
	v_pk_fma_f32 v[70:71], v[70:71], v[142:143], v[138:139] op_sel:[0,1,1] op_sel_hi:[1,1,1]
	v_max_f32_e32 v56, 0x358637bd, v56
	v_max_f32_e32 v64, 0x358637bd, v64
	v_max_f32_e32 v57, 0x358637bd, v57
	v_max_f32_e32 v65, 0x358637bd, v65
	v_max_f32_e32 v58, 0x358637bd, v58
	v_max_f32_e32 v66, 0x358637bd, v66
	v_max_f32_e32 v59, 0x358637bd, v59
	v_max_f32_e32 v67, 0x358637bd, v67
	v_max_f32_e32 v60, 0x358637bd, v60
	v_max_f32_e32 v68, 0x358637bd, v68
	v_max_f32_e32 v61, 0x358637bd, v61
	v_max_f32_e32 v69, 0x358637bd, v69
	v_max_f32_e32 v62, 0x358637bd, v62
	v_max_f32_e32 v70, 0x358637bd, v70
	v_max_f32_e32 v63, 0x358637bd, v63
	v_max_f32_e32 v71, 0x358637bd, v71
	v_log_f32_e32 v78, v56
	v_log_f32_e32 v86, v64
	v_log_f32_e32 v79, v57
	v_log_f32_e32 v87, v65
	v_log_f32_e32 v80, v58
	v_log_f32_e32 v88, v66
	v_log_f32_e32 v81, v59
	v_log_f32_e32 v89, v67
	v_log_f32_e32 v82, v60
	v_log_f32_e32 v90, v68
	v_log_f32_e32 v83, v61
	v_log_f32_e32 v91, v69
	v_log_f32_e32 v84, v62
	v_log_f32_e32 v92, v70
	v_log_f32_e32 v85, v63
	v_log_f32_e32 v93, v71
	v_pk_add_f32 v[2:3], 1.0, v[56:57] op_sel_hi:[0,1] neg_lo:[0,1] neg_hi:[0,1]
	v_pk_add_f32 v[10:11], 1.0, v[64:65] op_sel_hi:[0,1] neg_lo:[0,1] neg_hi:[0,1]
	v_pk_add_f32 v[4:5], 1.0, v[58:59] op_sel_hi:[0,1] neg_lo:[0,1] neg_hi:[0,1]
	v_pk_add_f32 v[12:13], 1.0, v[66:67] op_sel_hi:[0,1] neg_lo:[0,1] neg_hi:[0,1]
	v_pk_add_f32 v[6:7], 1.0, v[60:61] op_sel_hi:[0,1] neg_lo:[0,1] neg_hi:[0,1]
	v_pk_add_f32 v[14:15], 1.0, v[68:69] op_sel_hi:[0,1] neg_lo:[0,1] neg_hi:[0,1]
	v_pk_add_f32 v[8:9], 1.0, v[62:63] op_sel_hi:[0,1] neg_lo:[0,1] neg_hi:[0,1]
	v_pk_add_f32 v[16:17], 1.0, v[70:71] op_sel_hi:[0,1] neg_lo:[0,1] neg_hi:[0,1]
	v_add_f32_e32 v220, v78, v195
	v_add_f32_e32 v232, 0, v86
	v_add_f32_e32 v221, v220, v79
	v_add_f32_e32 v233, v232, v87
	v_add_f32_e32 v222, v221, v80
	v_add_f32_e32 v234, v233, v88
	v_add_f32_e32 v223, v222, v81
	v_add_f32_e32 v235, v234, v89
	v_add_f32_e32 v224, v223, v82
	v_add_f32_e32 v236, v235, v90
	v_add_f32_e32 v225, v224, v83
	v_add_f32_e32 v237, v236, v91
	v_add_f32_e32 v226, v225, v84
	v_add_f32_e32 v238, v237, v92
	v_add_f32_e32 v227, v226, v85
	v_add_f32_e32 v239, v238, v93
	v_mov_b32_e32 v76, v227
	v_mov_b32_e32 v77, v239

.LBB0_472:
	s_mov_b64 s[8:9], -1
	s_and_b64 vcc, exec, s[78:79]
	v_add_u32_e32 v72, 0, v103
	v_add_u32_e32 v153, s1, v108
	s_cbranch_vccnz .LBB0_474
	v_add_u32_e32 v74, 0x1a000, v72
	ds_read2st64_b64 v[160:163], v74 offset1:1
	ds_read2st64_b64 v[164:167], v74 offset0:2 offset1:3
	ds_read2st64_b64 v[168:171], v74 offset0:4 offset1:5
	ds_read2st64_b64 v[172:175], v74 offset0:6 offset1:7
	s_mov_b64 s[8:9], 0
	s_waitcnt lgkmcnt(0)
	v_pk_add_f32 v[74:75], v[160:161], 0 op_sel_hi:[1,0]
	s_nop 0
	v_cndmask_b32_e64 v81, 0, v74, s[60:61]
	v_cndmask_b32_e64 v79, 0, v75, s[60:61]
	v_add_f32_e32 v83, v162, v81
	v_add_f32_e32 v85, v163, v79
	v_cndmask_b32_e64 v81, v81, v83, s[62:63]
	v_cndmask_b32_e64 v79, v79, v85, s[62:63]
	v_add_f32_e32 v83, v164, v81
	v_add_f32_e32 v85, v165, v79
	v_cndmask_b32_e64 v81, v81, v83, s[64:65]
	v_pk_add_f32 v[74:75], v[74:75], v[162:163]
	v_cndmask_b32_e64 v79, v79, v85, s[64:65]
	v_add_f32_e32 v83, v166, v81
	v_pk_add_f32 v[74:75], v[74:75], v[164:165]
	v_add_f32_e32 v85, v167, v79
	v_cndmask_b32_e64 v81, v81, v83, s[66:67]
	v_cndmask_b32_e64 v79, v79, v85, s[66:67]
	v_pk_add_f32 v[160:161], v[74:75], v[166:167]
	v_add_f32_e32 v74, v168, v81
	v_add_f32_e32 v75, v169, v79
	v_cndmask_b32_e64 v81, v81, v74, s[68:69]
	v_cndmask_b32_e64 v79, v79, v75, s[68:69]
	v_add_f32_e32 v83, v170, v81
	v_add_f32_e32 v85, v171, v79
	v_cndmask_b32_e64 v81, v81, v83, s[70:71]
	v_cndmask_b32_e64 v79, v79, v85, s[70:71]
	v_add_f32_e32 v83, v172, v81
	v_add_f32_e32 v85, v173, v79
	v_cndmask_b32_e64 v81, v81, v83, s[72:73]
	v_cndmask_b32_e64 v79, v79, v85, s[72:73]
	v_add_f32_e32 v83, v174, v81
	v_add_f32_e32 v85, v175, v79
	v_cndmask_b32_e64 v154, v81, v83, s[74:75]
	v_cndmask_b32_e64 v155, v79, v85, s[74:75]
	v_pk_add_f32 v[74:75], v[160:161], v[168:169]
	v_pk_add_f32 v[220:221], v[220:221], v[154:155] op_sel_hi:[1,0]
	v_pk_add_f32 v[232:233], v[232:233], v[154:155] op_sel:[0,1] op_sel_hi:[1,1]
	v_pk_add_f32 v[222:223], v[222:223], v[154:155] op_sel_hi:[1,0]
	v_pk_add_f32 v[234:235], v[234:235], v[154:155] op_sel:[0,1] op_sel_hi:[1,1]
	v_pk_add_f32 v[224:225], v[224:225], v[154:155] op_sel_hi:[1,0]
	v_pk_add_f32 v[236:237], v[236:237], v[154:155] op_sel:[0,1] op_sel_hi:[1,1]
	v_pk_add_f32 v[226:227], v[226:227], v[154:155] op_sel_hi:[1,0]
	v_pk_add_f32 v[238:239], v[238:239], v[154:155] op_sel:[0,1] op_sel_hi:[1,1]
	v_pk_add_f32 v[74:75], v[74:75], v[170:171]
	v_pk_add_f32 v[220:221], v[220:221], v[160:161] op_sel_hi:[1,0] neg_lo:[0,1] neg_hi:[0,1]
	v_pk_add_f32 v[232:233], v[232:233], v[160:161] op_sel:[0,1] op_sel_hi:[1,1] neg_lo:[0,1] neg_hi:[0,1]
	v_pk_add_f32 v[222:223], v[222:223], v[160:161] op_sel_hi:[1,0] neg_lo:[0,1] neg_hi:[0,1]
	v_pk_add_f32 v[234:235], v[234:235], v[160:161] op_sel:[0,1] op_sel_hi:[1,1] neg_lo:[0,1] neg_hi:[0,1]
	v_pk_add_f32 v[224:225], v[224:225], v[160:161] op_sel_hi:[1,0] neg_lo:[0,1] neg_hi:[0,1]
	v_pk_add_f32 v[236:237], v[236:237], v[160:161] op_sel:[0,1] op_sel_hi:[1,1] neg_lo:[0,1] neg_hi:[0,1]
	v_pk_add_f32 v[226:227], v[226:227], v[160:161] op_sel_hi:[1,0] neg_lo:[0,1] neg_hi:[0,1]
	v_pk_add_f32 v[238:239], v[238:239], v[160:161] op_sel:[0,1] op_sel_hi:[1,1] neg_lo:[0,1] neg_hi:[0,1]
	v_pk_add_f32 v[74:75], v[74:75], v[172:173]
	v_med3_f32 v220, v220, s12, v228
	v_med3_f32 v221, v221, s12, v228
	v_med3_f32 v232, v232, s12, v228
	v_med3_f32 v233, v233, s12, v228
	v_med3_f32 v222, v222, s12, v228
	v_med3_f32 v223, v223, s12, v228
	v_med3_f32 v234, v234, s12, v228
	v_med3_f32 v235, v235, s12, v228
	v_med3_f32 v224, v224, s12, v228
	v_med3_f32 v225, v225, s12, v228
	v_med3_f32 v236, v236, s12, v228
	v_med3_f32 v237, v237, s12, v228
	v_med3_f32 v226, v226, s12, v228
	v_med3_f32 v227, v227, s12, v228
	v_med3_f32 v238, v238, s12, v228
	v_med3_f32 v239, v239, s12, v228
	v_pk_add_f32 v[74:75], v[74:75], v[174:175]
	v_add_u32_e32 v166, 0x4400, v153
	v_add_u32_e32 v167, 0x400, v153
	v_pk_add_f32 v[162:163], v[74:75], v[160:161] neg_lo:[0,1] neg_hi:[0,1]
	v_exp_f32_e32 v220, v220
	v_exp_f32_e32 v221, v221
	v_exp_f32_e32 v232, v232
	v_exp_f32_e32 v233, v233
	v_exp_f32_e32 v222, v222
	v_exp_f32_e32 v223, v223
	v_exp_f32_e32 v234, v234
	v_exp_f32_e32 v235, v235
	v_exp_f32_e32 v224, v224
	v_exp_f32_e32 v225, v225
	v_exp_f32_e32 v236, v236
	v_exp_f32_e32 v237, v237
	v_exp_f32_e32 v226, v226
	v_exp_f32_e32 v227, v227
	v_exp_f32_e32 v238, v238
	v_exp_f32_e32 v239, v239
	v_exp_f32_e32 v156, v162
	v_exp_f32_e32 v157, v163
	v_add_u32_e32 v168, 0x4800, v153
	v_rcp_f32_e32 v176, v220
	v_rcp_f32_e32 v177, v221
	v_rcp_f32_e32 v184, v232
	v_rcp_f32_e32 v185, v233
	v_rcp_f32_e32 v178, v222
	v_rcp_f32_e32 v179, v223
	v_rcp_f32_e32 v186, v234
	v_rcp_f32_e32 v187, v235
	v_rcp_f32_e32 v180, v224
	v_rcp_f32_e32 v181, v225
	v_rcp_f32_e32 v188, v236
	v_rcp_f32_e32 v189, v237
	v_rcp_f32_e32 v182, v226
	v_rcp_f32_e32 v183, v227
	v_rcp_f32_e32 v190, v238
	v_rcp_f32_e32 v191, v239
	v_pk_mul_f32 v[220:221], v[200:201], v[220:221]
	v_pk_mul_f32 v[232:233], v[208:209], v[232:233]
	v_pk_mul_f32 v[222:223], v[202:203], v[222:223]
	v_pk_mul_f32 v[234:235], v[210:211], v[234:235]
	v_pk_mul_f32 v[224:225], v[204:205], v[224:225]
	v_pk_mul_f32 v[236:237], v[212:213], v[236:237]
	v_pk_mul_f32 v[226:227], v[206:207], v[226:227]
	v_pk_mul_f32 v[238:239], v[214:215], v[238:239]
	v_pk_mul_f32 v[78:79], v[176:177], v[156:157] op_sel_hi:[1,0]
	v_pk_mul_f32 v[80:81], v[184:185], v[156:157] op_sel:[0,1] op_sel_hi:[1,1]
	v_pk_mul_f32 v[82:83], v[178:179], v[156:157] op_sel_hi:[1,0]
	v_pk_mul_f32 v[84:85], v[186:187], v[156:157] op_sel:[0,1] op_sel_hi:[1,1]
	v_pk_mul_f32 v[86:87], v[180:181], v[156:157] op_sel_hi:[1,0]
	v_pk_mul_f32 v[88:89], v[188:189], v[156:157] op_sel:[0,1] op_sel_hi:[1,1]
	v_pk_mul_f32 v[90:91], v[182:183], v[156:157] op_sel_hi:[1,0]
	v_pk_mul_f32 v[92:93], v[190:191], v[156:157] op_sel:[0,1] op_sel_hi:[1,1]
	v_pk_mul_f32 v[176:177], v[2:3], v[176:177]
	v_pk_mul_f32 v[184:185], v[10:11], v[184:185]
	v_pk_mul_f32 v[178:179], v[4:5], v[178:179]
	v_pk_mul_f32 v[186:187], v[12:13], v[186:187]
	v_pk_mul_f32 v[180:181], v[6:7], v[180:181]
	v_pk_mul_f32 v[188:189], v[14:15], v[188:189]
	v_pk_mul_f32 v[182:183], v[8:9], v[182:183]
	v_pk_mul_f32 v[190:191], v[16:17], v[190:191]
	v_pk_mul_f32 v[78:79], v[2:3], v[78:79]
	v_pk_mul_f32 v[80:81], v[10:11], v[80:81]
	v_pk_mul_f32 v[82:83], v[4:5], v[82:83]
	v_pk_mul_f32 v[84:85], v[12:13], v[84:85]
	v_pk_mul_f32 v[86:87], v[6:7], v[86:87]
	v_pk_mul_f32 v[88:89], v[14:15], v[88:89]
	v_pk_mul_f32 v[90:91], v[8:9], v[90:91]
	v_pk_mul_f32 v[92:93], v[16:17], v[92:93]
	v_cvt_pk_bf16_f32 v158, v220, v232
	v_cvt_pk_bf16_f32 v159, v221, v233
	v_cvt_pk_bf16_f32 v164, v222, v234
	v_cvt_pk_bf16_f32 v165, v223, v235
	v_cvt_pk_bf16_f32 v169, v224, v236
	v_cvt_pk_bf16_f32 v170, v225, v237
	v_cvt_pk_bf16_f32 v171, v226, v238
	v_cvt_pk_bf16_f32 v172, v227, v239
	ds_write2_b32 v153, v158, v159 offset1:68
	ds_write2_b32 v153, v164, v165 offset0:136 offset1:204
	ds_write2_b32 v167, v169, v170 offset0:16 offset1:84
	ds_write2_b32 v167, v171, v172 offset0:152 offset1:220
	v_cvt_pk_bf16_f32 v173, v176, v184
	v_cvt_pk_bf16_f32 v174, v177, v185
	v_cvt_pk_bf16_f32 v175, v178, v186
	v_cvt_pk_bf16_f32 v162, v179, v187
	v_cvt_pk_bf16_f32 v163, v180, v188
	v_cvt_pk_bf16_f32 v154, v181, v189
	v_cvt_pk_bf16_f32 v155, v182, v190
	v_cvt_pk_bf16_f32 v160, v183, v191
	ds_write2_b32 v166, v173, v174 offset1:68
	ds_write2_b32 v166, v175, v162 offset0:136 offset1:204
	ds_write2_b32 v168, v163, v154 offset0:16 offset1:84
	ds_write2_b32 v168, v155, v160 offset0:152 offset1:220
